# v47_touch_early
# speedup vs baseline: 1.0063x; 1.0063x over previous
_Z10k_enc_scanPKDF16_PKfS2_S2_S2_S2_S2_S2_S2_S2_S2_S0_S2_S2_S2_S2_S2_S0_S2_PfPjS2_S2_S2_S2_S2_S2_S2_S2_S2_S2_S2_S2_PDF16_S5_S3_:
	s_load_dwordx4 s[52:55], s[0:1], 0x98
	s_cmp_gt_u32 s2, 15
	s_mov_b64 s[4:5], -1
	s_cbranch_scc0 .LBB3_39
	s_add_i32 s3, s2, -16
	s_cmpk_gt_i32 s3, 0x33f
	s_cbranch_scc1 .LBB3_38
	v_add_u32_e32 v5, 0x140, v0
	v_add_u32_e32 v6, 0x280, v0
	v_mul_u32_u24_e32 v3, 0x5f5, v5
	v_add_u32_e32 v7, 0x3c0, v0
	v_lshrrev_b32_e32 v10, 17, v3
	v_mul_u32_u24_e32 v3, 0xbe9, v6
	v_add_u32_e32 v8, 0x500, v0
	v_lshrrev_b32_e32 v11, 18, v3
	v_mul_u32_u24_e32 v3, 0xbe9, v7
	v_add_u32_e32 v2, 0x640, v0
	v_lshrrev_b32_e32 v12, 18, v3
	v_mul_u32_u24_e32 v3, 0xbe9, v8
	s_load_dwordx2 s[20:21], s[0:1], 0x90
	s_load_dwordx4 s[56:59], s[0:1], 0x80
	s_load_dwordx8 s[12:19], s[0:1], 0x60
	s_load_dwordx8 s[24:31], s[0:1], 0x40
	s_load_dwordx8 s[36:43], s[0:1], 0x0
	s_load_dwordx8 s[44:51], s[0:1], 0x20
	v_lshrrev_b32_e32 v14, 18, v3
	v_mul_u32_u24_e32 v3, 0x17d1, v2
	s_movk_i32 s4, 0xffaa
	v_lshrrev_b32_e32 v16, 19, v3
	v_mad_i32_i24 v116, v16, s4, v2
	v_mul_u32_u24_e32 v2, 22, v0
	v_mov_b32_e32 v67, 0
	v_lshlrev_b32_e32 v66, 2, v2
	v_mul_u32_u24_e32 v2, 11, v0
	s_waitcnt lgkmcnt(0)
	v_lshl_add_u64 v[72:73], s[40:41], 0, v[66:67]
	v_lshlrev_b32_e32 v66, 2, v2
	v_lshrrev_b32_e32 v2, 1, v0
	v_lshl_add_u64 v[76:77], s[44:45], 0, v[66:67]
	v_and_b32_e32 v117, 0xfc, v2
	v_and_b32_e32 v2, 0x1c0, v0
	s_movk_i32 s8, 0xc0
	v_add_u32_e32 v66, 0xffffff40, v0
	v_cmp_eq_u32_e64 s[8:9], s8, v2
	v_lshlrev_b64 v[2:3], 2, v[66:67]
	v_lshl_add_u64 v[88:89], s[14:15], 0, v[2:3]
	v_lshl_add_u64 v[90:91], s[56:57], 0, v[2:3]
	v_lshl_add_u64 v[92:93], s[12:13], 0, v[2:3]
	v_lshl_add_u64 v[94:95], s[18:19], 0, v[2:3]
	v_lshl_add_u64 v[96:97], s[16:17], 0, v[2:3]
	v_mul_u32_u24_e32 v2, 0x5556, v0
	v_mov_b32_e32 v3, -3
	s_movk_i32 s18, 0x1a0
	v_mul_i32_i24_sdwa v3, v2, v3 dst_sel:DWORD dst_unused:UNUSED_PAD src0_sel:WORD_1 src1_sel:DWORD
	v_mul_u32_u24_sdwa v19, v2, s18 dst_sel:DWORD dst_unused:UNUSED_PAD src0_sel:WORD_1 src1_sel:DWORD
	v_mul_u32_u24_e32 v2, 0xa3e, v0
	v_lshrrev_b32_e32 v2, 12, v2
	v_mad_i32_i24 v112, v10, s4, v5
	v_mad_i32_i24 v113, v11, s4, v6
	v_mad_i32_i24 v114, v12, s4, v7
	v_mad_i32_i24 v115, v14, s4, v8
	v_add_lshl_u32 v20, v3, v0, 4
	v_mul_u32_u24_e32 v3, 0xa3e, v5
	v_mul_u32_u24_e32 v5, 0xa3e, v6
	v_mul_u32_u24_e32 v6, 0xa3e, v7
	v_mul_u32_u24_e32 v7, 0xa3e, v8
	v_and_b32_e32 v2, 0x1f0, v2
	v_lshlrev_b32_e32 v8, 4, v0
	v_add_u32_e32 v123, v2, v8
	v_lshrrev_b32_e32 v2, 12, v3
	v_and_b32_e32 v2, 0x3f0, v2
	v_add_u32_e32 v124, v2, v8
	v_lshrrev_b32_e32 v2, 12, v5
	v_and_b32_e32 v2, 0x7f0, v2
	v_add_u32_e32 v125, v2, v8
	v_lshrrev_b32_e32 v2, 12, v6
	v_and_b32_e32 v2, 0x7f0, v2
	v_mul_u32_u24_e32 v1, 0x2fb, v0
	v_add_u32_e32 v126, v2, v8
	v_lshrrev_b32_e32 v2, 12, v7
	v_and_b32_e32 v4, 63, v0
	v_lshrrev_b32_e32 v9, 16, v1
	v_and_b32_e32 v2, 0x7f0, v2
	v_mad_i32_i24 v1, v9, s4, v0
	v_and_b32_e32 v18, 15, v0
	v_add_u32_e32 v127, v2, v8
	v_lshrrev_b32_e32 v2, 2, v0
	s_movk_i32 s19, 0x70
	v_and_b32_e32 v98, 48, v0
	v_lshlrev_b32_e32 v66, 4, v4
	v_mov_b32_e32 v99, v67
	v_mov_b32_e32 v4, 0xfffff920
	v_and_or_b32 v128, v2, s19, v18
	v_lshl_add_u64 v[102:103], s[20:21], 0, v[98:99]
	v_mad_u64_u32 v[2:3], s[20:21], s2, 22, v[0:1]
	v_mov_b32_e32 v5, -1
	v_mad_u64_u32 v[104:105], s[20:21], v2, 5, v[4:5]
	v_min_u32_e32 v13, 21, v12
	v_min_u32_e32 v15, 21, v14
	v_min_u32_e32 v17, 21, v16
	s_movk_i32 s20, 0x410
	v_mov_b32_e32 v2, 0xfffa6a00
	v_mad_u32_u24 v99, v17, s20, v2
	v_mad_u32_u24 v105, v15, s20, v2
	v_mad_u32_u24 v130, v13, s20, v2
	v_mad_u32_u24 v131, v11, s20, v2
	v_mad_u32_u24 v132, v10, s20, v2
	v_mad_u32_u24 v133, v9, s20, v2
	v_lshlrev_b32_e32 v2, 6, v0
	s_mul_i32 s20, s2, 0x42000
	v_and_b32_e32 v2, 0x7000, v2
	v_add_u32_e32 v2, s20, v2
	v_lshlrev_b32_e32 v3, 8, v18
	v_lshlrev_b32_e32 v68, 2, v0
	v_mov_b32_e32 v69, v67
	s_movk_i32 s6, 0xb0
	s_movk_i32 s10, 0x102
	v_mul_lo_u32 v21, v1, s18
	v_lshlrev_b32_e32 v22, 4, v9
	v_mul_lo_u32 v23, v112, s18
	v_lshlrev_b32_e32 v24, 4, v10
	v_mul_lo_u32 v25, v113, s18
	v_lshlrev_b32_e32 v26, 4, v11
	s_movk_i32 s12, 0x3a4
	v_mul_lo_u32 v27, v114, s18
	v_lshlrev_b32_e32 v12, 4, v12
	s_movk_i32 s14, 0x264
	v_mul_lo_u32 v28, v115, s18
	v_lshlrev_b32_e32 v14, 4, v14
	s_movk_i32 s16, 0x124
	v_mul_lo_u32 v29, v116, s18
	v_lshlrev_b32_e32 v16, 4, v16
	v_mul_u32_u24_e32 v6, 0x1a0, v128
	v_or3_b32 v2, v2, v3, v98
	v_lshlrev_b32_e32 v106, 4, v0
	v_cmp_gt_u32_e64 s[22:23], 22, v0
	v_cmp_gt_u32_e64 s[4:5], 11, v0
	v_lshl_add_u64 v[70:71], s[42:43], 0, v[68:69]
	v_lshl_add_u64 v[74:75], s[46:47], 0, v[68:69]
	v_cmp_gt_u32_e64 s[6:7], s6, v0
	v_lshl_add_u64 v[78:79], s[50:51], 0, v[68:69]
	v_lshl_add_u64 v[80:81], s[28:29], 0, v[68:69]
	v_lshl_add_u64 v[82:83], s[48:49], 0, v[68:69]
	v_lshl_add_u64 v[84:85], s[26:27], 0, v[68:69]
	v_lshl_add_u64 v[86:87], s[24:25], 0, v[68:69]
	v_cmp_gt_u32_e64 s[10:11], s10, v0
	s_mov_b64 s[98:99], exec
	s_and_b64 exec, s[98:99], s[4:5]
	global_load_dword v244, v[70:71], off
	global_load_dword v245, v[72:73], off
	global_load_dword v246, v[72:73], off offset:64
	s_and_b64 exec, s[98:99], s[22:23]
	global_load_dword v247, v[76:77], off
	global_load_dword v248, v[74:75], off
	s_and_b64 exec, s[98:99], s[6:7]
	global_load_dword v249, v[80:81], off
	global_load_dword v250, v[78:79], off
	global_load_dword v251, v[82:83], off
	global_load_dword v252, v[84:85], off
	global_load_dword v253, v[86:87], off
	s_and_b64 exec, s[98:99], s[22:23]
	v_mov_b32_e32 v254, v104
	v_ashrrev_i32_e32 v255, 31, v104
	v_lshl_add_u64 v[254:255], v[254:255], 2, s[38:39]
	global_load_dword v244, v[254:255], off
	global_load_dword v245, v[254:255], off offset:16
	s_and_b64 exec, s[98:99], s[8:9]
	global_load_dword v246, v[90:91], off
	global_load_dword v247, v[88:89], off
	global_load_dword v248, v[92:93], off
	global_load_dword v249, v[94:95], off
	global_load_dword v250, v[96:97], off
	s_mov_b64 exec, s[98:99]
	v_lshlrev_b32_e32 v69, 5, v9
	v_lshlrev_b32_e32 v118, 5, v10
	v_lshlrev_b32_e32 v119, 5, v11
	v_cmp_gt_u32_e64 s[12:13], s12, v0
	v_lshlrev_b32_e32 v120, 5, v13
	v_cmp_gt_u32_e64 s[14:15], s14, v0
	v_lshlrev_b32_e32 v121, 5, v15
	v_cmp_gt_u32_e64 s[16:17], s16, v0
	v_lshlrev_b32_e32 v122, 5, v17
	v_mad_u32_u24 v129, v18, s18, v98
	s_mov_b32 s27, 0x20000
	s_mov_b32 s26, 0x1080000
	s_and_b32 s25, s53, 0xffff
	s_mov_b32 s24, s52
	v_lshl_add_u64 v[100:101], s[58:59], 0, v[66:67]
	v_cmp_eq_u32_e64 s[18:19], 0, v0
	s_mul_i32 s29, s2, 0x5960
	s_movk_i32 s33, 0x7000
	v_add_u32_e32 v134, 0xffbe0000, v2
	v_mov_b32_e32 v108, v106
	v_mov_b32_e32 v109, v67
	s_movk_i32 s35, 0x1000
	s_movk_i32 s41, 0x2000
	s_movk_i32 s43, 0x3000
	s_movk_i32 s45, 0x5000
	s_movk_i32 s47, 0x6000
	s_mov_b32 s49, 0x8000
	s_mov_b32 s60, 0xa000
	s_mov_b32 s61, 0xb000
	s_mov_b32 s28, 0x3f3504f3
	s_mov_b32 s62, 0x378e98ab
	s_mov_b32 s63, 0x3b7cd369
	s_mov_b32 s64, 0xbcc618b2
	s_mov_b32 s65, 0x3dda74e4
	s_mov_b32 s66, 0x3f228afd
	s_mov_b32 s67, 0x3e03c728
	s_mov_b32 s68, 0xbfb8aa3b
	s_mov_b32 s69, 0x42ce8ed0
	s_mov_b32 s70, 0xc2b17218
	v_mov_b32_e32 v135, 0x3ba10414
	s_brev_b32 s71, -2
	s_mov_b32 s72, 0xf800000
	v_mov_b32_e32 v136, 0x260
	v_add_u32_e32 v137, v19, v20
	s_movk_i32 s73, 0x401
	s_mov_b32 s74, 0x3ea7ba05
	s_mov_b32 s34, 0xbfba00e3
	s_mov_b32 s40, 0x3f87dc22
	s_mov_b32 s42, 0x3fb5f0e3
	v_add_u32_e32 v138, v21, v22
	v_add_u32_e32 v139, v23, v24
	v_add_u32_e32 v140, v25, v26
	v_add_u32_e32 v141, v27, v12
	v_add_u32_e32 v142, v28, v14
	v_add_u32_e32 v143, v29, v16
	v_add_u32_e32 v144, v98, v6
	s_mov_b32 s75, 0x12000
	s_mov_b32 s76, 0x14000
	s_mov_b32 s77, 0x15000
	s_mov_b32 s78, 0x16000
	s_mov_b32 s79, 0x17000
	s_mov_b32 s80, 0x19000
	s_mov_b32 s81, 0x1a000
	s_mov_b32 s82, 0x1b000
	s_mov_b32 s83, 0x1c000
	s_mov_b32 s84, 0x1e000
	s_mov_b32 s85, 0x1f000
	s_mov_b32 s86, 0x21000
	s_mov_b32 s87, 0x23000
	s_mov_b32 s88, 0x24000
	s_mov_b32 s89, 0x25000
	s_mov_b32 s90, 0x26000
	s_mov_b32 s91, 0x28000
	s_mov_b32 s92, 0x29000
	s_mov_b32 s93, 0x2a000
	v_mov_b32_e32 v145, 1
	v_mov_b32_e32 v146, 0xb9c68948
	v_mov_b32_e32 v147, 0x7f800000
	v_mov_b32_e32 v148, v67
	v_mov_b32_e32 v149, v67
	v_mov_b32_e32 v150, v67
	v_mov_b32_e32 v151, v67
	s_mov_b32 s44, 0xbe91a98e
	s_mov_b32 s46, 0x3e827906
	s_mov_b32 s48, 0x4038aa3b
	s_branch .LBB3_4
